# routing token scatter: both token-choices of a thread processed side by side (one pointer fetch, both TOPI loads in flight together, no store waits)
# speedup vs baseline: 1.0003x; 1.0003x over previous
.LBB0_1699:
	s_load_dwordx2 s[12:13], s[0:1], 0x118
	s_movk_i32 s16, 0x1100
	v_ashrrev_i32_e32 v3, 2, v2
	v_add_u32_e32 v3, s11, v3
	v_ashrrev_i32_e32 v4, 12, v3
	v_and_b32_e32 v5, 0xfff, v3
	v_mad_i32_i24 v4, v4, s16, v5
	v_cndmask_b32_e64 v3, v4, v3, s[4:5]
	v_lshl_or_b32 v4, v3, 2, v0
	v_ashrrev_i32_e32 v5, 31, v4
	v_lshlrev_b64 v[4:5], 2, v[4:5]
	v_add_u32_e32 v10, 0x200, v2
	v_ashrrev_i32_e32 v11, 2, v10
	v_add_u32_e32 v11, s11, v11
	v_ashrrev_i32_e32 v12, 12, v11
	v_and_b32_e32 v13, 0xfff, v11
	v_mad_i32_i24 v12, v12, s16, v13
	v_cndmask_b32_e64 v11, v12, v11, s[4:5]
	v_lshl_or_b32 v12, v11, 2, v0
	v_ashrrev_i32_e32 v13, 31, v12
	v_lshlrev_b64 v[12:13], 2, v[12:13]
	v_cmp_gt_i32_e64 s[8:9], s10, v10
	s_waitcnt lgkmcnt(0)
	v_lshl_add_u64 v[6:7], s[12:13], 0, v[4:5]
	v_add_co_u32_e32 v6, vcc, s85, v6
	s_nop 1
	v_addc_co_u32_e32 v7, vcc, 0, v7, vcc
	global_load_dword v6, v[6:7], off
	s_mov_b64 s[14:15], exec
	s_and_b64 exec, exec, s[8:9]
	s_cbranch_execz .Lroute_nob1
	v_lshl_add_u64 v[14:15], s[12:13], 0, v[12:13]
	v_add_co_u32_e32 v14, vcc, s85, v14
	s_nop 1
	v_addc_co_u32_e32 v15, vcc, 0, v15, vcc
	global_load_dword v14, v[14:15], off
.Lroute_nob1:
	s_mov_b64 exec, s[14:15]
	s_waitcnt vmcnt(0)
	v_lshl_add_u32 v6, v6, 2, 0
	v_add_u32_e32 v16, 0x201a0, v6
	ds_add_rtn_u32 v16, v16, v205
	v_add_u32_e32 v17, 0x20100, v6
	v_add_u32_e32 v6, 0x20080, v6
	ds_read_b32 v17, v17
	ds_read_b32 v6, v6
	s_waitcnt lgkmcnt(0)
	v_add3_u32 v6, v17, v16, v6
	v_ashrrev_i32_e32 v7, 31, v6
	v_lshl_add_u64 v[8:9], v[6:7], 2, s[12:13]
	v_add_co_u32_e32 v8, vcc, 0xc00000, v8
	s_nop 1
	v_addc_co_u32_e32 v9, vcc, 0, v9, vcc
	global_store_dword v[8:9], v3, off
	v_lshl_add_u64 v[4:5], s[12:13], 0, v[4:5]
	v_add_co_u32_e32 v4, vcc, 0xb00000, v4
	s_nop 1
	v_addc_co_u32_e32 v5, vcc, 0, v5, vcc
	global_store_dword v[4:5], v6, off
	s_and_b64 exec, exec, s[8:9]
	s_cbranch_execz .Lroute_nob2
	v_lshl_add_u32 v14, v14, 2, 0
	v_add_u32_e32 v16, 0x201a0, v14
	ds_add_rtn_u32 v16, v16, v205
	v_add_u32_e32 v17, 0x20100, v14
	v_add_u32_e32 v14, 0x20080, v14
	ds_read_b32 v17, v17
	ds_read_b32 v14, v14
	s_waitcnt lgkmcnt(0)
	v_add3_u32 v14, v17, v16, v14
	v_ashrrev_i32_e32 v15, 31, v14
	v_lshl_add_u64 v[18:19], v[14:15], 2, s[12:13]
	v_add_co_u32_e32 v18, vcc, 0xc00000, v18
	s_nop 1
	v_addc_co_u32_e32 v19, vcc, 0, v19, vcc
	global_store_dword v[18:19], v11, off
	v_lshl_add_u64 v[12:13], s[12:13], 0, v[12:13]
	v_add_co_u32_e32 v12, vcc, 0xb00000, v12
	s_nop 1
	v_addc_co_u32_e32 v13, vcc, 0, v13, vcc
	global_store_dword v[12:13], v14, off
.Lroute_nob2:
	s_mov_b64 exec, s[14:15]
